# LDS-DMA staging extended to 14 of 16 Wv fragments per wave (3 more in the idle Xh/Oh/H1 LDS area)
# baseline (speedup 1.0000x reference)
.Lring_go_0:
	v_mul_f32_e32 v74, v10, v70
	v_mul_f32_e32 v75, v6, v70
	v_mul_f32_e32 v76, v10, v66
	v_mul_f32_e32 v77, v6, v66
	v_mul_f32_e32 v78, v10, v62
	v_mul_f32_e32 v79, v6, v62
	v_mul_f32_e32 v80, v10, v58
	v_mul_f32_e32 v81, v6, v58
	v_mul_f32_e32 v82, v10, v54
	v_mul_f32_e32 v83, v6, v54
	v_mul_f32_e32 v84, v10, v46
	v_mul_f32_e32 v85, v6, v46
	v_mul_f32_e32 v86, v10, v34
	v_mul_f32_e32 v87, v6, v34
	v_mul_f32_e32 v88, v10, v14
	v_mul_f32_e32 v89, v6, v14
	v_fmac_f32_e32 v74, v71, v11
	v_fmac_f32_e32 v75, v71, v7
	v_fmac_f32_e32 v76, v67, v11
	v_fmac_f32_e32 v77, v67, v7
	v_fmac_f32_e32 v78, v63, v11
	v_fmac_f32_e32 v79, v63, v7
	v_fmac_f32_e32 v80, v59, v11
	v_fmac_f32_e32 v81, v59, v7
	v_fmac_f32_e32 v82, v55, v11
	v_fmac_f32_e32 v83, v55, v7
	v_fmac_f32_e32 v84, v47, v11
	v_fmac_f32_e32 v85, v47, v7
	v_fmac_f32_e32 v86, v35, v11
	v_fmac_f32_e32 v87, v35, v7
	v_fmac_f32_e32 v88, v15, v11
	v_fmac_f32_e32 v89, v15, v7
	v_fmac_f32_e32 v74, v72, v12
	v_fmac_f32_e32 v75, v72, v8
	v_fmac_f32_e32 v76, v68, v12
	v_fmac_f32_e32 v77, v68, v8
	v_fmac_f32_e32 v78, v64, v12
	v_fmac_f32_e32 v79, v64, v8
	v_fmac_f32_e32 v80, v60, v12
	v_fmac_f32_e32 v81, v60, v8
	v_fmac_f32_e32 v82, v56, v12
	v_fmac_f32_e32 v83, v56, v8
	v_fmac_f32_e32 v84, v48, v12
	v_fmac_f32_e32 v85, v48, v8
	v_fmac_f32_e32 v86, v36, v12
	v_fmac_f32_e32 v87, v36, v8
	v_fmac_f32_e32 v88, v16, v12
	v_fmac_f32_e32 v89, v16, v8
	v_fmac_f32_e32 v74, v73, v13
	v_fmac_f32_e32 v75, v73, v9
	v_fmac_f32_e32 v76, v69, v13
	v_fmac_f32_e32 v77, v69, v9
	v_fmac_f32_e32 v78, v65, v13
	v_fmac_f32_e32 v79, v65, v9
	v_fmac_f32_e32 v80, v61, v13
	v_fmac_f32_e32 v81, v61, v9
	v_fmac_f32_e32 v82, v57, v13
	v_fmac_f32_e32 v83, v57, v9
	v_fmac_f32_e32 v84, v49, v13
	v_fmac_f32_e32 v85, v49, v9
	v_fmac_f32_e32 v86, v37, v13
	v_fmac_f32_e32 v87, v37, v9
	v_fmac_f32_e32 v88, v17, v13
	v_fmac_f32_e32 v89, v17, v9
	v_permlane32_swap_b32_e32 v74, v82
	v_permlane32_swap_b32_e32 v75, v83
	v_permlane32_swap_b32_e32 v76, v84
	v_permlane32_swap_b32_e32 v77, v85
	v_permlane32_swap_b32_e32 v78, v86
	v_permlane32_swap_b32_e32 v79, v87
	v_permlane32_swap_b32_e32 v80, v88
	v_permlane32_swap_b32_e32 v81, v89
	v_add_f32_e32 v74, v74, v82
	v_add_f32_e32 v75, v75, v83
	v_add_f32_e32 v76, v76, v84
	v_add_f32_e32 v77, v77, v85
	v_add_f32_e32 v78, v78, v86
	v_add_f32_e32 v79, v79, v87
	v_add_f32_e32 v80, v80, v88
	v_add_f32_e32 v81, v81, v89
	v_permlane16_swap_b32_e32 v74, v78
	v_permlane16_swap_b32_e32 v75, v79
	v_permlane16_swap_b32_e32 v76, v80
	v_permlane16_swap_b32_e32 v77, v81
	v_add_f32_e32 v74, v74, v78
	v_add_f32_e32 v75, v75, v79
	v_add_f32_e32 v76, v76, v80
	v_add_f32_e32 v77, v77, v81
	v_add_f32_dpp v74, v74, v74 row_ror:8 row_mask:0xf bank_mask:0xf bound_ctrl:1
	v_add_f32_dpp v76, v76, v76 row_ror:8 row_mask:0xf bank_mask:0xf bound_ctrl:1
	v_add_f32_dpp v75, v75, v75 row_ror:8 row_mask:0xf bank_mask:0xf bound_ctrl:1
	v_add_f32_dpp v77, v77, v77 row_ror:8 row_mask:0xf bank_mask:0xf bound_ctrl:1
	v_cndmask_b32_e64 v74, v76, v74, s[4:5]
	v_cndmask_b32_e64 v75, v77, v75, s[4:5]
	v_cmp_eq_u32_e64 s[0:1], 0, v107
	v_add_f32_dpp v74, v74, v74 row_half_mirror row_mask:0xf bank_mask:0xf bound_ctrl:1
	v_add_f32_dpp v75, v75, v75 row_half_mirror row_mask:0xf bank_mask:0xf bound_ctrl:1
	v_cndmask_b32_e64 v74, v75, v74, s[2:3]
	s_nop 1
	v_add_f32_dpp v74, v74, v74 quad_perm:[2,3,0,1] row_mask:0xf bank_mask:0xf bound_ctrl:1
	s_nop 1
	v_add_f32_dpp v74, v74, v74 quad_perm:[1,0,3,2] row_mask:0xf bank_mask:0xf bound_ctrl:1
	v_cndmask_b32_e64 v74, v113, v74, s[0:1]
	s_and_saveexec_b64 s[0:1], vcc
	ds_write_b32 v114, v74
	s_or_b64 exec, exec, s[0:1]
	v_mov_b32_dpp v90, v74 row_ror:8 row_mask:0xf bank_mask:0xf bound_ctrl:1
	v_add_u32_e32 v114, 32, v114
	v_max_f32_e32 v90, v74, v90
	v_mov_b32_e32 v91, v90
	s_nop 1
	v_permlane16_swap_b32_e32 v90, v91
	s_nop 0
	v_max_f32_e32 v90, v90, v91
	v_mov_b32_e32 v91, v90
	s_nop 1
	v_permlane32_swap_b32_e32 v90, v91
	s_nop 0
	v_max3_f32 v92, v104, v90, v91
	v_sub_f32_e32 v93, v104, v92
	v_sub_f32_e32 v94, v74, v92
	v_exp_f32_e32 v93, v93
	v_exp_f32_e32 v94, v94
	v_mov_b32_e32 v104, v92
	s_nop 1
	v_fma_f32 v105, v105, v93, v94
	s_nop 0
	v_readlane_b32 s34, v93, 0
	v_readlane_b32 s36, v93, 4
	v_readlane_b32 s38, v94, 0
	v_readlane_b32 s40, v94, 4
	v_readlane_b32 s42, v94, 8
	v_readlane_b32 s44, v94, 12
	v_readlane_b32 s46, v94, 16
	v_readlane_b32 s48, v94, 20
	v_readlane_b32 s50, v94, 24
	v_readlane_b32 s52, v94, 28
	v_readlane_b32 s54, v94, 32
	v_readlane_b32 s56, v94, 36
	v_readlane_b32 s58, v94, 40
	v_readlane_b32 s60, v94, 44
	v_readlane_b32 s62, v94, 48
	v_readlane_b32 s64, v94, 52
	v_readlane_b32 s66, v94, 56
	v_readlane_b32 s68, v94, 60
	s_nop 1
	v_pk_mul_f32 v[96:97], v[96:97], s[34:35] op_sel_hi:[1,0]
	v_pk_mul_f32 v[98:99], v[98:99], s[34:35] op_sel_hi:[1,0]
	v_pk_mul_f32 v[100:101], v[100:101], s[36:37] op_sel_hi:[1,0]
	v_pk_mul_f32 v[102:103], v[102:103], s[36:37] op_sel_hi:[1,0]
	v_pk_fma_f32 v[96:97], v[70:71], s[38:39], v[96:97] op_sel_hi:[1,0,1]
	v_pk_fma_f32 v[98:99], v[72:73], s[38:39], v[98:99] op_sel_hi:[1,0,1]
	v_pk_fma_f32 v[100:101], v[70:71], s[40:41], v[100:101] op_sel_hi:[1,0,1]
	v_pk_fma_f32 v[102:103], v[72:73], s[40:41], v[102:103] op_sel_hi:[1,0,1]
	v_pk_fma_f32 v[96:97], v[66:67], s[42:43], v[96:97] op_sel_hi:[1,0,1]
	v_pk_fma_f32 v[98:99], v[68:69], s[42:43], v[98:99] op_sel_hi:[1,0,1]
	v_pk_fma_f32 v[100:101], v[66:67], s[44:45], v[100:101] op_sel_hi:[1,0,1]
	v_pk_fma_f32 v[102:103], v[68:69], s[44:45], v[102:103] op_sel_hi:[1,0,1]
	v_pk_fma_f32 v[96:97], v[62:63], s[46:47], v[96:97] op_sel_hi:[1,0,1]
	v_pk_fma_f32 v[98:99], v[64:65], s[46:47], v[98:99] op_sel_hi:[1,0,1]
	v_pk_fma_f32 v[100:101], v[62:63], s[48:49], v[100:101] op_sel_hi:[1,0,1]
	v_pk_fma_f32 v[102:103], v[64:65], s[48:49], v[102:103] op_sel_hi:[1,0,1]
	v_pk_fma_f32 v[96:97], v[58:59], s[50:51], v[96:97] op_sel_hi:[1,0,1]
	v_pk_fma_f32 v[98:99], v[60:61], s[50:51], v[98:99] op_sel_hi:[1,0,1]
	v_pk_fma_f32 v[100:101], v[58:59], s[52:53], v[100:101] op_sel_hi:[1,0,1]
	v_pk_fma_f32 v[102:103], v[60:61], s[52:53], v[102:103] op_sel_hi:[1,0,1]
	v_pk_fma_f32 v[96:97], v[54:55], s[54:55], v[96:97] op_sel_hi:[1,0,1]
	v_pk_fma_f32 v[98:99], v[56:57], s[54:55], v[98:99] op_sel_hi:[1,0,1]
	v_pk_fma_f32 v[100:101], v[54:55], s[56:57], v[100:101] op_sel_hi:[1,0,1]
	v_pk_fma_f32 v[102:103], v[56:57], s[56:57], v[102:103] op_sel_hi:[1,0,1]
	v_pk_fma_f32 v[96:97], v[46:47], s[58:59], v[96:97] op_sel_hi:[1,0,1]
	v_pk_fma_f32 v[98:99], v[48:49], s[58:59], v[98:99] op_sel_hi:[1,0,1]
	v_pk_fma_f32 v[100:101], v[46:47], s[60:61], v[100:101] op_sel_hi:[1,0,1]
	v_pk_fma_f32 v[102:103], v[48:49], s[60:61], v[102:103] op_sel_hi:[1,0,1]
	v_pk_fma_f32 v[96:97], v[34:35], s[62:63], v[96:97] op_sel_hi:[1,0,1]
	v_pk_fma_f32 v[98:99], v[36:37], s[62:63], v[98:99] op_sel_hi:[1,0,1]
	v_pk_fma_f32 v[100:101], v[34:35], s[64:65], v[100:101] op_sel_hi:[1,0,1]
	v_pk_fma_f32 v[102:103], v[36:37], s[64:65], v[102:103] op_sel_hi:[1,0,1]
	v_pk_fma_f32 v[96:97], v[14:15], s[66:67], v[96:97] op_sel_hi:[1,0,1]
	v_pk_fma_f32 v[98:99], v[16:17], s[66:67], v[98:99] op_sel_hi:[1,0,1]
	v_pk_fma_f32 v[100:101], v[14:15], s[68:69], v[100:101] op_sel_hi:[1,0,1]
	v_pk_fma_f32 v[102:103], v[16:17], s[68:69], v[102:103] op_sel_hi:[1,0,1]
	s_cmp_lg_u32 s30, 8
	s_cbranch_scc1 .Lring_nostage
	v_lshlrev_b32_e32 v176, 4, v196
	v_lshl_add_u32 v176, v197, 14, v176
	s_mov_b32 m0, s33
	s_nop 0
	global_load_lds_dwordx4 v176, s[8:9]
	global_load_lds_dwordx4 v176, s[8:9] offset:1024
	global_load_lds_dwordx4 v176, s[8:9] offset:2048
	global_load_lds_dwordx4 v176, s[8:9] offset:3072
	v_add_u32_e32 v176, 0x1000, v176
	s_add_u32 s35, s33, 4096
	s_mov_b32 m0, s35
	s_nop 0
	global_load_lds_dwordx4 v176, s[8:9]
	global_load_lds_dwordx4 v176, s[8:9] offset:1024
	global_load_lds_dwordx4 v176, s[8:9] offset:2048
	global_load_lds_dwordx4 v176, s[8:9] offset:3072
	v_add_u32_e32 v176, 0x1000, v176
	s_add_u32 s35, s33, 8192
	s_mov_b32 m0, s35
	s_nop 0
	global_load_lds_dwordx4 v176, s[8:9]
	global_load_lds_dwordx4 v176, s[8:9] offset:1024
	global_load_lds_dwordx4 v176, s[8:9] offset:2048
	v_add_u32_e32 v176, 0xc00, v176
	s_mul_i32 s35, s32, 3072
	s_add_u32 s35, s35, 46080
	s_mov_b32 m0, s35
	s_nop 0
	global_load_lds_dwordx4 v176, s[8:9]
	global_load_lds_dwordx4 v176, s[8:9] offset:1024
	global_load_lds_dwordx4 v176, s[8:9] offset:2048

.Lring_done:
	s_setprio 0
	v_mov_b32_e32 v240, v96
	v_mov_b32_e32 v241, v97
	v_mov_b32_e32 v242, v98
	v_mov_b32_e32 v243, v99
	v_mov_b32_e32 v244, v100
	v_mov_b32_e32 v245, v101
	v_mov_b32_e32 v246, v102
	v_mov_b32_e32 v247, v103
	v_mov_b32_e32 v248, v104
	v_mov_b32_e32 v249, v105
	s_movk_i32 s0, 0x640
	v_mov_b32_e32 v14, 0x8200
	v_mad_u32_u24 v205, v197, s0, v14
	v_lshlrev_b32_e32 v10, 4, v106
	v_or_b32_e32 v6, 0x2000, v196
	v_add_lshl_u32 v7, v122, v6, 4
	v_lshlrev_b32_e32 v11, 4, v196
	v_add_u32_e32 v11, s33, v11
	s_mul_i32 s35, s32, 3072
	s_add_u32 s35, s35, 46080
	v_lshlrev_b32_e32 v12, 4, v196
	v_add_u32_e32 v12, s35, v12
	ds_read_b128 v[158:161], v11
	ds_read_b128 v[154:157], v11 offset:1024
	ds_read_b128 v[146:149], v11 offset:2048
	ds_read_b128 v[138:141], v11 offset:3072
	ds_read_b128 v[118:121], v11 offset:4096
	ds_read_b128 v[106:109], v11 offset:5120
	ds_read_b128 v[98:101], v11 offset:6144
	ds_read_b128 v[102:105], v11 offset:7168
	ds_read_b128 v[170:173], v11 offset:8192
	ds_read_b128 v[166:169], v11 offset:9216
	ds_read_b128 v[178:181], v11 offset:10240
	ds_read_b128 v[174:177], v12
	ds_read_b128 v[162:165], v12 offset:1024
	s_nop 0
	ds_read_b128 v[134:137], v12 offset:2048
	global_load_dwordx4 v[114:117], v145, s[8:9]
	global_load_dwordx4 v[110:113], v150, s[8:9]
	global_load_dwordx4 v[94:97], v7, s[8:9]
	global_load_dwordx4 v[90:93], v7, s[8:9] offset:1024
	global_load_dwordx4 v[78:81], v7, s[8:9] offset:2048
	global_load_dwordx4 v[74:77], v7, s[8:9] offset:3072
	v_add_lshl_u32 v7, v123, v6, 4
	v_add_lshl_u32 v8, v124, v6, 4
	global_load_dwordx4 v[66:69], v7, s[8:9]
	global_load_dwordx4 v[58:61], v8, s[8:9]
	v_add_lshl_u32 v7, v125, v6, 4
	v_add_lshl_u32 v8, v126, v6, 4
	global_load_dwordx4 v[62:65], v7, s[8:9]
	global_load_dwordx4 v[54:57], v8, s[8:9]
	v_add_lshl_u32 v7, v127, v6, 4
	v_add_lshl_u32 v8, v128, v6, 4
	global_load_dwordx4 v[150:153], v7, s[8:9]
	global_load_dwordx4 v[142:145], v8, s[8:9]
	v_add_lshl_u32 v7, v129, v6, 4
	v_add_lshl_u32 v8, v130, v6, 4
	global_load_dwordx4 v[130:133], v7, s[8:9]
	global_load_dwordx4 v[126:129], v8, s[8:9]
	v_add_lshl_u32 v7, v192, v6, 4
	v_add_lshl_u32 v8, v202, v6, 4
	global_load_dwordx4 v[122:125], v7, s[8:9]
	global_load_dwordx4 v[82:85], v8, s[8:9]
	v_add_lshl_u32 v7, v203, v6, 4
	v_add_lshl_u32 v6, v204, v6, 4
	global_load_dwordx4 v[86:89], v7, s[8:9]
	global_load_dwordx4 v[70:73], v6, s[8:9]
	v_lshlrev_b32_e32 v187, 2, v195
	v_and_or_b32 v190, v187, 4, s31
	v_or_b32_e32 v208, 1, v190
	v_mul_u32_u24_e32 v6, 0x300, v197
	v_ashrrev_i32_e32 v191, 31, v190
	v_ashrrev_i32_e32 v209, 31, v208
	v_or_b32_e32 v6, v196, v6
	v_lshlrev_b64 v[210:211], 9, v[190:191]
	v_lshlrev_b32_e32 v191, 2, v1
	v_lshlrev_b64 v[222:223], 9, v[208:209]
	v_or_b32_e32 v208, 2, v190
	v_mov_b32_e32 v193, 0
	v_lshlrev_b32_e32 v14, 4, v6
	v_lshl_or_b32 v192, v197, 7, v191
	s_movk_i32 s2, 0xfe00
	v_ashrrev_i32_e32 v209, 31, v208
	v_or_b32_e32 v6, 0x40000, v14
	s_movk_i32 s1, 0x100
	v_lshl_add_u64 v[220:221], s[22:23], 0, v[192:193]
	s_mov_b32 s3, -1
	v_lshlrev_b64 v[226:227], 9, v[208:209]
	v_or_b32_e32 v208, 3, v190
	global_load_dwordx4 v[50:53], v6, s[8:9]
	global_load_dwordx4 v[46:49], v6, s[8:9] offset:1024
	global_load_dwordx4 v[42:45], v6, s[8:9] offset:2048
	global_load_dwordx4 v[30:33], v6, s[8:9] offset:3072
	v_add_u32_e32 v6, 0x41000, v14
	v_add_u32_e32 v7, 0x41400, v14
	v_lshl_add_u64 v[212:213], s[20:21], 0, v[192:193]
	v_lshl_add_u64 v[202:203], v[220:221], 0, s[2:3]
	v_cmp_gt_u32_e32 vcc, s1, v0
	v_ashrrev_i32_e32 v209, 31, v208
	s_movk_i32 s2, 0xfe40
	global_load_dwordx4 v[38:41], v6, s[8:9]
	global_load_dwordx4 v[22:25], v7, s[8:9]
	v_add_u32_e32 v6, 0x41800, v14
	v_add_u32_e32 v7, 0x41c00, v14
	v_cndmask_b32_e32 v203, v203, v213, vcc
	v_cndmask_b32_e32 v202, v202, v212, vcc
	v_lshlrev_b64 v[230:231], 9, v[208:209]
	s_mov_b32 s3, -1
	global_load_dwordx4 v[34:37], v6, s[8:9]
	global_load_dwordx4 v[10:13], v7, s[8:9]
	v_add_u32_e32 v6, 0x42000, v14
	v_add_u32_e32 v7, 0x42400, v14
	v_add_u32_e32 v15, 0x42800, v14
	v_add_u32_e32 v18, 0x42c00, v14
	v_lshl_add_u64 v[206:207], v[202:203], 0, v[210:211]
	v_lshl_add_u64 v[224:225], v[202:203], 0, v[222:223]
	v_lshl_add_u64 v[228:229], v[202:203], 0, v[226:227]
	v_lshl_add_u64 v[202:203], v[202:203], 0, v[230:231]
	v_lshl_add_u64 v[212:213], v[212:213], 0, 64
	v_lshl_add_u64 v[220:221], v[220:221], 0, s[2:3]
	global_load_dwordx4 v[26:29], v6, s[8:9]
	s_nop 0
	global_load_dwordx4 v[6:9], v7, s[8:9]
	s_nop 0
	global_load_dwordx4 v[14:17], v15, s[8:9]
	s_nop 0
	global_load_dwordx4 v[18:21], v18, s[8:9]
	s_nop 0
	global_load_dword v208, v[206:207], off
	s_nop 0
	global_load_dword v207, v[224:225], off
	global_load_dword v204, v[228:229], off
	s_nop 0
	global_load_dword v203, v[202:203], off
	s_nop 0
	global_load_dword v206, v192, s[10:11]
	global_load_dword v202, v192, s[10:11] offset:64
	v_cndmask_b32_e32 v213, v221, v213, vcc
	v_cndmask_b32_e32 v212, v220, v212, vcc
	v_lshl_add_u64 v[210:211], v[212:213], 0, v[210:211]
	v_lshl_add_u64 v[220:221], v[212:213], 0, v[222:223]
	v_lshl_add_u64 v[222:223], v[212:213], 0, v[226:227]
	v_lshl_add_u64 v[224:225], v[212:213], 0, v[230:231]
	global_load_dword v212, v[210:211], off
	s_nop 0
	global_load_dword v211, v[220:221], off
	global_load_dword v210, v[222:223], off
	global_load_dword v209, v[224:225], off
	v_lshl_or_b32 v190, v197, 4, v1
	v_lshlrev_b32_e32 v186, 2, v190
	global_load_dword v189, v186, s[24:25]
	global_load_dword v188, v186, s[26:27]
	v_mov_b32_e32 v233, v249
	v_mov_b32_e32 v232, v248
	v_mov_b32_e32 v214, v240
	v_mov_b32_e32 v215, v241
	v_mov_b32_e32 v216, v242
	v_mov_b32_e32 v217, v243
	v_mov_b32_e32 v218, v244
	v_mov_b32_e32 v219, v245
	v_mov_b32_e32 v220, v246
	v_mov_b32_e32 v221, v247
	s_nop 1
	v_add_f32_dpp v2, v233, v233 row_ror:8 row_mask:0xf bank_mask:0xf bound_ctrl:1
	v_mov_b32_e32 v3, v2
	s_nop 1
	v_permlane16_swap_b32_e32 v2, v3
	v_add_f32_e32 v2, v2, v3
	v_mov_b32_e32 v3, v2
	s_nop 1
	v_permlane32_swap_b32_e32 v2, v3
	v_add_f32_e32 v2, v2, v3
	v_readlane_b32 s2, v232, 4
	v_readlane_b32 s4, v2, 4
	v_readlane_b32 s5, v2, 0
	v_readlane_b32 s3, v232, 0
	v_div_scale_f32 v3, s[0:1], s4, s4, 1.0
	v_rcp_f32_e32 v4, v3
	v_lshl_add_u64 v[182:183], v[182:183], 2, s[28:29]
	v_fma_f32 v2, -v3, v4, 1.0
	v_fmac_f32_e32 v4, v2, v4
	v_div_scale_f32 v2, vcc, 1.0, s4, 1.0
	v_mul_f32_e32 v5, v2, v4
	v_fma_f32 v192, -v3, v5, v2
	v_fmac_f32_e32 v5, v192, v4
	v_fma_f32 v2, -v3, v5, v2
	v_div_scale_f32 v3, s[0:1], s5, s5, 1.0
	v_rcp_f32_e32 v192, v3
	v_div_fmas_f32 v2, v2, v4, v5
	v_div_fixup_f32 v2, v2, s4, 1.0
	s_movk_i32 s0, 0xc8
	v_fma_f32 v4, -v3, v192, 1.0
	v_fmac_f32_e32 v192, v4, v192
	v_div_scale_f32 v4, vcc, 1.0, s5, 1.0
	v_mul_f32_e32 v5, v4, v192
	v_fma_f32 v213, -v3, v5, v4
	v_fmac_f32_e32 v5, v213, v192
	v_fma_f32 v3, -v3, v5, v4
	v_div_fmas_f32 v3, v3, v192, v5
	v_div_fixup_f32 v4, v3, s5, 1.0
	v_pk_mul_f32 v[216:217], v[216:217], v[4:5] op_sel_hi:[1,0]
	v_pk_mul_f32 v[214:215], v[214:215], v[4:5] op_sel_hi:[1,0]
	v_cvt_pk_f16_f32 v217, v216, v217
	v_cvt_pk_f16_f32 v216, v214, v215
	v_pk_mul_f32 v[214:215], v[220:221], v[2:3] op_sel_hi:[1,0]
	v_pk_mul_f32 v[218:219], v[218:219], v[2:3] op_sel_hi:[1,0]
	v_add_u32_e32 v3, v205, v184
	ds_read2_b32 v[220:221], v3 offset0:128 offset1:200
	v_cvt_pk_f16_f32 v215, v214, v215
	v_cvt_pk_f16_f32 v214, v218, v219
	ds_read2st64_b32 v[218:219], v3 offset1:1
	v_add_u32_e32 v192, 32, v3
	ds_write2st64_b64 v185, v[216:217], v[214:215] offset1:1
	ds_read2st64_b32 v[214:215], v192 offset0:4 offset1:5
	s_waitcnt lgkmcnt(3)
	v_subrev_f32_e32 v5, s2, v221
	v_exp_f32_e32 v5, v5
	s_waitcnt lgkmcnt(2)
	v_subrev_f32_e32 v185, s3, v218
	v_exp_f32_e32 v185, v185
	s_waitcnt lgkmcnt(0)
	v_subrev_f32_e32 v205, s2, v214
	v_mul_f32_e32 v5, v2, v5
	v_subrev_f32_e32 v192, s3, v219
	v_exp_f32_e32 v205, v205
	v_fmac_f32_e32 v5, v4, v185
	v_mov_b32_e32 v185, v193
	v_exp_f32_e32 v192, v192
	v_lshl_add_u64 v[182:183], v[182:183], 0, v[184:185]
	v_subrev_f32_e32 v185, s2, v215
	v_mul_f32_e32 v5, 0.5, v5
	v_subrev_f32_e32 v184, s3, v220
	v_exp_f32_e32 v185, v185
	global_store_dword v[182:183], v5, off
	v_mul_f32_e32 v5, v2, v205
	v_exp_f32_e32 v184, v184
	v_fmac_f32_e32 v5, v4, v192
	v_mul_f32_e32 v5, 0.5, v5
	global_store_dword v[182:183], v5, off offset:256
	v_mul_f32_e32 v5, v2, v185
	v_fmac_f32_e32 v5, v4, v184
	v_mul_f32_e32 v5, 0.5, v5
	global_store_dword v[182:183], v5, off offset:512
	v_or_b32_e32 v5, 0xc0, v196
	v_cmp_gt_u32_e32 vcc, s0, v5
	s_and_saveexec_b64 s[0:1], vcc
	s_cbranch_execz .LBB1_19
	v_add_u32_e32 v3, 0x300, v3
	ds_read2_b32 v[184:185], v3 offset1:200
	s_waitcnt lgkmcnt(0)
	v_subrev_f32_e32 v3, s3, v184
	v_subrev_f32_e32 v5, s2, v185
	v_exp_f32_e32 v184, v3
	v_exp_f32_e32 v185, v5
	v_mov_b32_e32 v5, v2
	v_pk_mul_f32 v[2:3], v[4:5], v[184:185]
	s_nop 0
	v_add_f32_e32 v2, v2, v3
	v_mul_f32_e32 v2, 0.5, v2
	global_store_dword v[182:183], v2, off offset:768
